# attention tile loops: role-split stagger - waves 0-3 issue their tile LDS reads before the next-tile LDS-DMA block, waves 4-7 keep DMA first, so the halves run offset without idling
# speedup vs baseline: 1.0029x; 1.0029x over previous
.LBB0_1652:
	s_or_b64 exec, exec, s[8:9]
	s_barrier
	v_readfirstlane_b32 s101, v0
	s_bitcmp1_b32 s101, 8
	s_cbranch_scc1 .Lmy_ma_late
	v_cmp_le_u32_e32 vcc, s17, v97
	s_cbranch_vccz .Lmy_ma_late
	s_lshl_b32 s10, s16, 14
	v_add3_u32 v2, s10, v93, v92
	v_add3_u32 v174, s10, v94, v92
	v_add3_u32 v175, s10, v95, v92
	v_add3_u32 v176, s10, v96, v92
	ds_read_b128 v[36:39], v2 offset:50048
	ds_read_b128 v[114:117], v174 offset:50048
	ds_read_b128 v[132:135], v175 offset:50048
	ds_read_b128 v[136:139], v176 offset:50048
	ds_read_b32 v177, v112
	ds_read2_b32 v[140:141], v113 offset0:26 offset1:27
	ds_read2_b32 v[142:143], v113 offset0:24 offset1:25
	ds_read2_b32 v[144:145], v113 offset0:18 offset1:19
	ds_read2_b32 v[146:147], v113 offset0:16 offset1:17
	ds_read2_b32 v[148:149], v113 offset0:10 offset1:11
	ds_read2_b32 v[150:151], v113 offset0:8 offset1:9
	ds_read2_b32 v[152:153], v113 offset0:2 offset1:3
	ds_read2_b32 v[154:155], v113 offset1:1
.Lmy_ma_late:
	s_add_i32 s8, s17, 5
	v_cmp_lt_u32_e32 vcc, s8, v100
	s_and_saveexec_b64 s[8:9], vcc
	s_cbranch_execz .LBB0_1654
	s_lshl_b32 s100, s16, 14
	s_addk_i32 s100, 0xc000
	s_cmp_lg_u32 s16, 0
	s_cselect_b32 s100, s100, 0x14000
	v_add_u32_e32 v196, s100, v106
	v_add_u32_e32 v197, 0xc380, v196
	v_add_u32_e32 v196, 0xe380, v196
	v_readfirstlane_b32 s100, v197
	s_mov_b32 m0, s100
	v_readfirstlane_b32 s100, v196
	global_load_lds_dwordx4 v[88:89], off
	v_lshl_add_u64 v[198:199], s[50:51], 1, v[86:87]
	s_mov_b32 m0, s100
	s_nop 0
	global_load_lds_dwordx4 v[198:199], off
.LBB0_1654:
	s_or_b64 exec, exec, s[8:9]
	v_cmp_le_u32_e32 vcc, s17, v97
	s_and_saveexec_b64 s[8:9], vcc
	s_cbranch_execz .LBB0_1635
	s_bitcmp1_b32 s101, 8
	s_cbranch_scc0 .Lmy_ma_have
	s_lshl_b32 s10, s16, 14
	v_add3_u32 v2, s10, v93, v92
	v_add3_u32 v174, s10, v94, v92
	v_add3_u32 v175, s10, v95, v92
	v_add3_u32 v176, s10, v96, v92
	ds_read_b128 v[36:39], v2 offset:50048
	ds_read_b128 v[114:117], v174 offset:50048
	ds_read_b128 v[132:135], v175 offset:50048
	ds_read_b128 v[136:139], v176 offset:50048
	ds_read_b32 v177, v112
	ds_read2_b32 v[140:141], v113 offset0:26 offset1:27
	ds_read2_b32 v[142:143], v113 offset0:24 offset1:25
	ds_read2_b32 v[144:145], v113 offset0:18 offset1:19
	ds_read2_b32 v[146:147], v113 offset0:16 offset1:17
	ds_read2_b32 v[148:149], v113 offset0:10 offset1:11
	ds_read2_b32 v[150:151], v113 offset0:8 offset1:9
	ds_read2_b32 v[152:153], v113 offset0:2 offset1:3
	ds_read2_b32 v[154:155], v113 offset1:1
.Lmy_ma_have:
	s_setprio 1
	s_waitcnt lgkmcnt(12)
	v_mfma_f32_32x32x16_bf16 v[36:51], v[36:39], v[52:55], 0
	s_waitcnt lgkmcnt(11)
	v_mfma_f32_32x32x16_bf16 v[36:51], v[114:117], v[56:59], v[36:51]
	s_waitcnt lgkmcnt(10)
	v_mfma_f32_32x32x16_bf16 v[36:51], v[132:135], v[60:63], v[36:51]
	s_waitcnt lgkmcnt(9)
	v_mfma_f32_32x32x16_bf16 v[36:51], v[136:139], v[64:67], v[36:51]
	s_setprio 0
	v_add3_u32 v174, s10, v98, v107
	v_add3_u32 v175, s10, v99, v107
	ds_read_b128 v[156:159], v174 offset:58240
	ds_read_b128 v[162:165], v174 offset:60288
	ds_read_b128 v[166:169], v175 offset:58240
	ds_read_b128 v[170:173], v175 offset:60288
	s_waitcnt lgkmcnt(4)
	v_lshrrev_b32_e32 v2, v102, v177
	v_bfe_i32 v178, v2, 0, 1
	v_bfe_i32 v179, v2, 1, 1
	v_bfe_i32 v180, v2, 2, 1
	v_bfe_i32 v181, v2, 3, 1
	v_bfe_i32 v182, v2, 8, 1
	v_bfe_i32 v183, v2, 9, 1
	v_bfe_i32 v184, v2, 10, 1
	v_bfe_i32 v185, v2, 11, 1
	v_bfe_i32 v186, v2, 16, 1
	v_bfe_i32 v187, v2, 17, 1
	v_bfe_i32 v188, v2, 18, 1
	v_bfe_i32 v189, v2, 19, 1
	v_bfe_i32 v190, v2, 24, 1
	v_bfe_i32 v191, v2, 25, 1
	v_bfe_i32 v192, v2, 26, 1
	v_bfe_i32 v193, v2, 27, 1
	v_pk_fma_f32 v[36:37], v[36:37], s[82:83], v[140:141] op_sel:[0,0,1] op_sel_hi:[1,0,0]
	v_pk_fma_f32 v[38:39], v[38:39], s[82:83], v[142:143] op_sel:[0,0,1] op_sel_hi:[1,0,0]
	v_bfi_b32 v36, v178, v36, v228
	v_bfi_b32 v37, v179, v37, v228
	v_bfi_b32 v38, v180, v38, v228
	v_bfi_b32 v39, v181, v39, v228
	v_max_f32_e32 v116, v36, v37
	v_max_f32_e32 v114, v38, v39
	v_max3_f32 v116, v116, s90, v114
	v_pk_fma_f32 v[40:41], v[40:41], s[82:83], v[144:145] op_sel:[0,0,1] op_sel_hi:[1,0,0]
	v_pk_fma_f32 v[42:43], v[42:43], s[82:83], v[146:147] op_sel:[0,0,1] op_sel_hi:[1,0,0]
	v_bfi_b32 v40, v182, v40, v228
	v_bfi_b32 v41, v183, v41, v228
	v_bfi_b32 v42, v184, v42, v228
	v_bfi_b32 v43, v185, v43, v228
	v_max_f32_e32 v117, v40, v41
	v_max_f32_e32 v114, v42, v43
	v_max3_f32 v116, v116, v117, v114
	v_pk_fma_f32 v[44:45], v[44:45], s[82:83], v[148:149] op_sel:[0,0,1] op_sel_hi:[1,0,0]
	v_pk_fma_f32 v[46:47], v[46:47], s[82:83], v[150:151] op_sel:[0,0,1] op_sel_hi:[1,0,0]
	v_bfi_b32 v44, v186, v44, v228
	v_bfi_b32 v45, v187, v45, v228
	v_bfi_b32 v46, v188, v46, v228
	v_bfi_b32 v47, v189, v47, v228
	v_max_f32_e32 v117, v44, v45
	v_max_f32_e32 v114, v46, v47
	v_max3_f32 v116, v116, v117, v114
	v_pk_fma_f32 v[48:49], v[48:49], s[82:83], v[152:153] op_sel:[0,0,1] op_sel_hi:[1,0,0]
	v_pk_fma_f32 v[50:51], v[50:51], s[82:83], v[154:155] op_sel:[0,0,1] op_sel_hi:[1,0,0]
	v_bfi_b32 v48, v190, v48, v228
	v_bfi_b32 v49, v191, v49, v228
	v_bfi_b32 v50, v192, v50, v228
	v_bfi_b32 v51, v193, v51, v228
	v_max_f32_e32 v117, v48, v49
	v_max_f32_e32 v2, v50, v51
	v_max3_f32 v2, v116, v117, v2
	v_mov_b32_e32 v114, v2
	v_mov_b32_e32 v115, v2
	s_nop 1
	v_permlane32_swap_b32_e32 v114, v115
	v_max3_f32 v2, v2, v114, v115
	v_add_f32_e32 v114, 0x41000000, v90
	v_cmp_gt_f32_e32 vcc, v2, v114
	s_cbranch_vccz .LBB0_1634
	v_max_f32_e32 v2, v2, v2
	v_max_f32_e32 v114, v90, v90
	v_max_f32_e32 v114, v114, v2
	v_sub_f32_e32 v2, v90, v114
	v_exp_f32_e32 v2, v2
	v_mov_b32_e32 v90, v114
	v_pk_mul_f32 v[34:35], v[34:35], v[2:3] op_sel_hi:[1,0]
	v_pk_mul_f32 v[32:33], v[32:33], v[2:3] op_sel_hi:[1,0]
	v_pk_mul_f32 v[30:31], v[30:31], v[2:3] op_sel_hi:[1,0]
	v_pk_mul_f32 v[28:29], v[28:29], v[2:3] op_sel_hi:[1,0]
	v_pk_mul_f32 v[26:27], v[26:27], v[2:3] op_sel_hi:[1,0]
	v_pk_mul_f32 v[24:25], v[24:25], v[2:3] op_sel_hi:[1,0]
	v_pk_mul_f32 v[22:23], v[22:23], v[2:3] op_sel_hi:[1,0]
	v_pk_mul_f32 v[20:21], v[20:21], v[2:3] op_sel_hi:[1,0]
	v_pk_mul_f32 v[18:19], v[18:19], v[2:3] op_sel_hi:[1,0]
	v_pk_mul_f32 v[16:17], v[16:17], v[2:3] op_sel_hi:[1,0]
	v_pk_mul_f32 v[14:15], v[14:15], v[2:3] op_sel_hi:[1,0]
	v_pk_mul_f32 v[12:13], v[12:13], v[2:3] op_sel_hi:[1,0]
	v_pk_mul_f32 v[10:11], v[10:11], v[2:3] op_sel_hi:[1,0]
	v_pk_mul_f32 v[8:9], v[8:9], v[2:3] op_sel_hi:[1,0]
	v_pk_mul_f32 v[6:7], v[6:7], v[2:3] op_sel_hi:[1,0]
	v_pk_mul_f32 v[4:5], v[4:5], v[2:3] op_sel_hi:[1,0]
	v_mul_f32_e32 v110, v110, v2
	s_branch .LBB0_1634

.LBB0_1707:
	s_or_b64 exec, exec, s[34:35]
	s_barrier
	v_readfirstlane_b32 s101, v0
	s_bitcmp1_b32 s101, 8
	s_cbranch_scc1 .Lmy_dl_late
	v_cmp_le_u32_e32 vcc, s49, v144
	s_cbranch_vccz .Lmy_dl_late
	s_lshl_b32 s36, s46, 14
	s_add_i32 s38, s36, 0
	v_add3_u32 v2, s38, v140, v139
	v_add3_u32 v202, s38, v141, v139
	v_add3_u32 v203, s38, v142, v139
	v_add3_u32 v204, s38, v143, v139
	ds_read_b128 v[36:39], v2 offset:16640
	ds_read_b128 v[52:55], v202 offset:16640
	ds_read_b128 v[178:181], v203 offset:16640
	ds_read_b128 v[182:185], v204 offset:16640
	v_add3_u32 v202, s38, v145, v152
	v_add3_u32 v203, s38, v146, v152
	ds_read_b128 v[186:189], v202 offset:24832
	ds_read_b128 v[190:193], v202 offset:26880
	ds_read_b128 v[194:197], v203 offset:24832
	ds_read_b128 v[198:201], v203 offset:26880

.LBB0_1709:
	s_or_b64 exec, exec, s[34:35]
	v_cmp_le_u32_e32 vcc, s49, v144
	s_and_saveexec_b64 s[34:35], vcc
	s_cbranch_execz .LBB0_1690
	s_bitcmp1_b32 s101, 8
	s_cbranch_scc0 .Lmy_dl_have
	s_lshl_b32 s36, s46, 14
	s_add_i32 s38, s36, 0
	v_add3_u32 v2, s38, v140, v139
	v_add3_u32 v202, s38, v141, v139
	v_add3_u32 v203, s38, v142, v139
	v_add3_u32 v204, s38, v143, v139
	ds_read_b128 v[36:39], v2 offset:16640
	ds_read_b128 v[52:55], v202 offset:16640
	ds_read_b128 v[178:181], v203 offset:16640
	ds_read_b128 v[182:185], v204 offset:16640
	v_add3_u32 v202, s38, v145, v152
	v_add3_u32 v203, s38, v146, v152
	ds_read_b128 v[186:189], v202 offset:24832
	ds_read_b128 v[190:193], v202 offset:26880
	ds_read_b128 v[194:197], v203 offset:24832
	ds_read_b128 v[198:201], v203 offset:26880
.Lmy_dl_have:
	s_setprio 1
	s_waitcnt lgkmcnt(7)
	v_mfma_f32_32x32x16_bf16 v[36:51], v[36:39], v[92:95], 0
	s_waitcnt lgkmcnt(6)
	v_mfma_f32_32x32x16_bf16 v[36:51], v[52:55], v[96:99], v[36:51]
	s_waitcnt lgkmcnt(5)
	v_mfma_f32_32x32x16_bf16 v[36:51], v[178:181], v[100:103], v[36:51]
	s_waitcnt lgkmcnt(4)
	v_mfma_f32_32x32x16_bf16 v[36:51], v[182:185], v[104:107], v[36:51]
	s_setprio 0
	s_mov_b64 s[36:37], -1
	s_cmp_ge_i32 s47, s42
	v_add_f32_e32 v159, 0x41000000, v158
	s_cbranch_scc0 .LBB0_1714
	v_add_u32_e32 v2, 0x1e7c, v156
	v_add_u32_e32 v205, 0x1e74, v156
	v_add_u32_e32 v56, 0x1e5c, v156
	v_add_u32_e32 v58, 0x1e54, v156
	ds_read2_b32 v[52:53], v2 offset1:1
	ds_read2_b32 v[54:55], v205 offset1:1
	ds_read2_b32 v[56:57], v56 offset1:1
	ds_read2_b32 v[58:59], v58 offset1:1
	v_add_u32_e32 v2, 0x1e3c, v156
	v_add_u32_e32 v205, 0x1e34, v156
	v_add_u32_e32 v235, 0x1e1c, v156
	v_add_u32_e32 v236, 0x1e14, v156
	ds_read2_b32 v[206:207], v2 offset1:1
	ds_read2_b32 v[208:209], v205 offset1:1
	ds_read2_b32 v[210:211], v235 offset1:1
	ds_read2_b32 v[212:213], v236 offset1:1
	s_waitcnt lgkmcnt(4)
	v_pk_fma_f32 v[130:131], v[36:37], s[82:83], v[52:53] op_sel:[0,0,1] op_sel_hi:[1,0,0]
	v_pk_fma_f32 v[88:89], v[38:39], s[82:83], v[54:55] op_sel:[0,0,1] op_sel_hi:[1,0,0]
	v_max_f32_e32 v2, v130, v131
	v_max_f32_e32 v52, v88, v89
	v_pk_fma_f32 v[86:87], v[40:41], s[82:83], v[56:57] op_sel:[0,0,1] op_sel_hi:[1,0,0]
	v_pk_fma_f32 v[84:85], v[42:43], s[82:83], v[58:59] op_sel:[0,0,1] op_sel_hi:[1,0,0]
	v_max3_f32 v2, v2, s90, v52
	v_max_f32_e32 v52, v86, v87
	v_max_f32_e32 v53, v84, v85
	v_max3_f32 v2, v2, v52, v53
	s_waitcnt lgkmcnt(0)
	v_pk_fma_f32 v[136:137], v[44:45], s[82:83], v[206:207] op_sel:[0,0,1] op_sel_hi:[1,0,0]
	v_mov_b32_e32 v160, v157
	v_pk_fma_f32 v[134:135], v[46:47], s[82:83], v[208:209] op_sel:[0,0,1] op_sel_hi:[1,0,0]
	v_max_f32_e32 v52, v136, v137
	v_max_f32_e32 v53, v134, v135
	v_pk_fma_f32 v[132:133], v[48:49], s[82:83], v[210:211] op_sel:[0,0,1] op_sel_hi:[1,0,0]
	v_pk_fma_f32 v[90:91], v[50:51], s[82:83], v[212:213] op_sel:[0,0,1] op_sel_hi:[1,0,0]
	v_max3_f32 v2, v2, v52, v53
	v_max_f32_e32 v52, v132, v133
	v_max_f32_e32 v53, v90, v91
	v_max3_f32 v2, v2, v52, v53
	v_mov_b32_e32 v52, v2
	v_mov_b32_e32 v53, v2
	s_nop 1
	v_permlane32_swap_b32_e32 v52, v53
	v_max3_f32 v161, v2, v52, v53
	v_cmp_gt_f32_e32 vcc, v161, v159
	v_mov_b32_e32 v2, v158
	s_cbranch_vccz .LBB0_1713
	v_max_f32_e32 v2, v161, v161
	v_max_f32_e32 v52, v158, v158
	v_max_f32_e32 v2, v52, v2
	v_sub_f32_e32 v52, v158, v2
	v_exp_f32_e32 v160, v52
	s_nop 0
	v_pk_mul_f32 v[34:35], v[34:35], v[160:161] op_sel_hi:[1,0]
	v_pk_mul_f32 v[32:33], v[32:33], v[160:161] op_sel_hi:[1,0]
	v_pk_mul_f32 v[30:31], v[30:31], v[160:161] op_sel_hi:[1,0]
	v_pk_mul_f32 v[28:29], v[28:29], v[160:161] op_sel_hi:[1,0]
	v_pk_mul_f32 v[26:27], v[26:27], v[160:161] op_sel_hi:[1,0]
	v_pk_mul_f32 v[24:25], v[24:25], v[160:161] op_sel_hi:[1,0]
	v_pk_mul_f32 v[22:23], v[22:23], v[160:161] op_sel_hi:[1,0]
	v_pk_mul_f32 v[20:21], v[20:21], v[160:161] op_sel_hi:[1,0]
	v_pk_mul_f32 v[18:19], v[18:19], v[160:161] op_sel_hi:[1,0]
	v_pk_mul_f32 v[16:17], v[16:17], v[160:161] op_sel_hi:[1,0]
	v_pk_mul_f32 v[14:15], v[14:15], v[160:161] op_sel_hi:[1,0]
	v_pk_mul_f32 v[12:13], v[12:13], v[160:161] op_sel_hi:[1,0]
	v_pk_mul_f32 v[10:11], v[10:11], v[160:161] op_sel_hi:[1,0]
	v_pk_mul_f32 v[8:9], v[8:9], v[160:161] op_sel_hi:[1,0]
	v_pk_mul_f32 v[6:7], v[6:7], v[160:161] op_sel_hi:[1,0]
	v_pk_mul_f32 v[4:5], v[4:5], v[160:161] op_sel_hi:[1,0]
	v_mul_f32_e32 v160, v157, v160
